# v7 + PROJ unit order rotated per XCD class (units 1..10): the 8 XCDs work on different 1024-column sections at the same time, so epilogue write bursts and the final L2 flush are spread
# speedup vs baseline: 1.0355x; 1.0258x over previous
.LBB0_278:
	s_add_i32 s48, s48, 1
	v_readlane_b32 s9, v255, 8
	s_mul_i32 s3, s48, s91
	s_mul_hi_u32 s8, s48, s9
	s_add_i32 s3, s8, s3
	s_mul_i32 s8, s48, s9
	s_add_u32 s8, s8, s94
	s_addc_u32 s9, s3, s92
	v_cmp_gt_i64_e32 vcc, s[8:9], v[208:209]
	v_cmp_lt_i64_e64 s[10:11], s[8:9], v[206:207]
	s_cbranch_vccnz .LBB0_280
	v_readlane_b32 s3, v255, 8
	s_nop 0
	s_cmp_lg_u32 s3, 0x100
	s_cbranch_scc1 .Lrot_skip
	s_and_b32 s3, s94, 7
	s_add_i32 s3, s3, s48
	s_sub_u32 s3, s3, 1
	s_cmp_ge_u32 s3, 10
	s_cbranch_scc0 .Lrot_nowrap
	s_sub_u32 s3, s3, 10
.Lrot_nowrap:
	s_add_u32 s3, s3, 1
	s_lshl_b32 s3, s3, 8
	s_add_u32 s8, s3, s94
.Lrot_skip:
	s_ashr_i32 s3, s8, 31
	s_lshr_b32 s3, s3, 29
	s_add_i32 s3, s8, s3
	s_ashr_i32 s9, s3, 3
	s_and_b32 s3, s3, -8
	s_sub_i32 s3, s8, s3
	s_cmp_lt_i32 s3, 0
	s_movk_i32 s8, 0x161
	s_cselect_b32 s8, s8, 0x160
	s_mul_i32 s3, s8, s3
	s_add_i32 s3, s3, s9
	s_mul_hi_i32 s8, s3, 0x2e8ba2e9
	s_lshr_b32 s9, s8, 31
	s_ashr_i32 s8, s8, 6
	s_add_i32 s8, s8, s9
	s_lshl_b32 s9, s8, 3
	s_sub_i32 s14, 64, s9
	s_min_i32 s14, s14, 8
	s_abs_i32 s15, s14
	v_cvt_f32_u32_e32 v2, s15
	s_sub_i32 s17, 0, s15
	s_mulk_i32 s8, 0x160
	s_sub_i32 s3, s3, s8
	v_rcp_iflag_f32_e32 v2, v2
	s_abs_i32 s8, s3
	s_xor_b32 s16, s3, s14
	s_ashr_i32 s16, s16, 31
	v_mul_f32_e32 v2, 0x4f7ffffe, v2
	v_cvt_u32_f32_e32 v2, v2
	s_nop 0
	v_readfirstlane_b32 s18, v2
	s_mul_i32 s17, s17, s18
	s_mul_hi_u32 s17, s18, s17
	s_add_i32 s18, s18, s17
	s_mul_hi_u32 s17, s8, s18
	s_mul_i32 s18, s17, s15
	s_sub_i32 s8, s8, s18
	s_add_i32 s19, s17, 1
	s_sub_i32 s18, s8, s15
	s_cmp_ge_u32 s8, s15
	s_cselect_b32 s17, s19, s17
	s_cselect_b32 s8, s18, s8
	s_add_i32 s18, s17, 1
	s_cmp_ge_u32 s8, s15
	s_cselect_b32 s8, s18, s17
	s_xor_b32 s8, s8, s16
	s_sub_i32 s70, s8, s16
	s_mul_i32 s8, s70, s14
	s_sub_i32 s3, s3, s8
	s_add_i32 s49, s3, s9
